# stack: early L1 invalidate in grid barrier + attention QK fragment reads issued up front + scan-A forward substitution with packed f32 FMAs and deep LDS prefetch
# speedup vs baseline: 1.0035x; 1.0035x over previous
; #define LAS __attribute__((address_space(3)))
; DI void phase_scan_a(Frame& F, int l, int u_lo, int u_hi, int u_step) {
;     ...
;             float Tc[32]; f32x4 rq[2][8];
; #pragma unroll
;             for (int q = 0; q < 1; ++q) rq[1][q] = *(const LAS f32x4*)(AD + 1 * 32 + 4 * q);
; #pragma unroll
;             for (int i = 0; i < 32; ++i) { float a0 = (i == cc) ? 1.f : 0.f, a1 = 0.f, a2 = 0.f, a3 = 0.f;
;                 if (i + 1 < 32 && i >= 1) {
; #pragma unroll
;                     for (int q = 0; q < (i + 1 + 3) / 4; ++q) rq[(i + 1) & 1][q] = *(const LAS f32x4*)(AD + (i + 1) * 32 + 4 * q); }
;                 __builtin_amdgcn_sched_barrier(0);
; #pragma unroll
;                 for (int q = 0; q < (i + 3) / 4; ++q) { const f32x4 a = rq[i & 1][q];
;                     if (4 * q + 0 < i) a0 += a[0] * Tc[4 * q + 0]; if (4 * q + 1 < i) a1 += a[1] * Tc[4 * q + 1]; if (4 * q + 2 < i) a2 += a[2] * Tc[4 * q + 2]; if (4 * q + 3 < i) a3 += a[3] * Tc[4 * q + 3]; }
;                 Tc[i] = (a0 + a1) + (a2 + a3);
;                 __builtin_amdgcn_sched_barrier(0); }
.LBB0_1132:
	s_and_b64 vcc, exec, s[40:41]
	s_cbranch_vccz .LBB0_1138
	s_nop 5
	v_mov_b32_e32 v68, v112
	ds_read_b128 v[20:23], v128 offset:128
	ds_read_b128 v[24:27], v128 offset:256
	ds_read_b128 v[28:31], v128 offset:384
	ds_read_b128 v[32:35], v128 offset:512
	ds_read_b128 v[36:39], v128 offset:640
	ds_read_b128 v[40:43], v128 offset:656
	ds_read_b128 v[44:47], v128 offset:768
	ds_read_b128 v[48:51], v128 offset:784
	ds_read_b128 v[52:55], v128 offset:896
	ds_read_b128 v[56:59], v128 offset:912
	ds_read_b128 v[60:63], v128 offset:1024
	ds_read_b128 v[100:103], v128 offset:1040
	ds_read_b128 v[202:205], v128 offset:1152
	ds_read_b128 v[226:229], v128 offset:1168
	ds_read_b128 v[234:237], v128 offset:1184
	s_waitcnt lgkmcnt(14)
	v_fma_f32 v69, v68, v20, v144
	s_waitcnt lgkmcnt(13)
	v_fma_f32 v66, v68, v24, v145
	v_fma_f32 v67, v69, v25, 0
	v_add_f32_e32 v70, v66, v67
	s_waitcnt lgkmcnt(12)
	v_fma_f32 v66, v68, v28, v146
	v_fma_f32 v67, v69, v29, 0
	v_fma_f32 v104, v70, v30, 0
	v_add_f32_e32 v66, v66, v67
	v_add_f32_e32 v71, v104, v66
	ds_read_b128 v[20:23], v128 offset:1280
	ds_read_b128 v[24:27], v128 offset:1296
	ds_read_b128 v[28:31], v128 offset:1312
	s_waitcnt lgkmcnt(14)
	v_fma_f32 v66, v68, v32, v147
	v_fma_f32 v67, v69, v33, 0
	v_pk_fma_f32 v[104:105], v[34:35], v[70:71], 0 op_sel_hi:[1,1,0]
	v_add_f32_e32 v66, v66, v67
	v_add_f32_e32 v104, v104, v105
	v_add_f32_e32 v72, v66, v104
	s_waitcnt lgkmcnt(12)
	v_fma_f32 v66, v68, v36, v148
	v_fma_f32 v67, v69, v37, 0
	v_pk_fma_f32 v[104:105], v[38:39], v[70:71], 0 op_sel_hi:[1,1,0]
	v_fmac_f32_e32 v66, v72, v40
	v_add_f32_e32 v66, v66, v67
	v_add_f32_e32 v104, v104, v105
	v_add_f32_e32 v73, v66, v104
	ds_read_b128 v[32:35], v128 offset:1408
	ds_read_b128 v[36:39], v128 offset:1424
	ds_read_b128 v[40:43], v128 offset:1440
	s_waitcnt lgkmcnt(13)
	v_fma_f32 v66, v68, v44, v149
	v_fma_f32 v67, v69, v45, 0
	v_pk_fma_f32 v[104:105], v[46:47], v[70:71], 0 op_sel_hi:[1,1,0]
	v_pk_fma_f32 v[66:67], v[48:49], v[72:73], v[66:67]
	v_add_f32_e32 v66, v66, v67
	v_add_f32_e32 v104, v104, v105
	v_add_f32_e32 v74, v66, v104
	s_waitcnt lgkmcnt(11)
	v_fma_f32 v66, v68, v52, v150
	v_fma_f32 v67, v69, v53, 0
	v_pk_fma_f32 v[104:105], v[54:55], v[70:71], 0 op_sel_hi:[1,1,0]
	v_pk_fma_f32 v[66:67], v[56:57], v[72:73], v[66:67]
	v_fmac_f32_e32 v104, v74, v58
	v_add_f32_e32 v66, v66, v67
	v_add_f32_e32 v104, v104, v105
	v_add_f32_e32 v75, v66, v104
	ds_read_b128 v[44:47], v128 offset:1536
	ds_read_b128 v[48:51], v128 offset:1552
	ds_read_b128 v[52:55], v128 offset:1568
	s_waitcnt lgkmcnt(12)
	v_fma_f32 v66, v68, v60, v151
	v_fma_f32 v67, v69, v61, 0
	v_pk_fma_f32 v[104:105], v[62:63], v[70:71], 0 op_sel_hi:[1,1,0]
	v_pk_fma_f32 v[66:67], v[100:101], v[72:73], v[66:67]
	v_pk_fma_f32 v[104:105], v[102:103], v[74:75], v[104:105]
	v_add_f32_e32 v66, v66, v67
	v_add_f32_e32 v104, v104, v105
	v_add_f32_e32 v76, v66, v104
	s_waitcnt lgkmcnt(9)
	v_fma_f32 v66, v68, v202, v152
	v_fma_f32 v67, v69, v203, 0
	v_pk_fma_f32 v[104:105], v[204:205], v[70:71], 0 op_sel_hi:[1,1,0]
	v_pk_fma_f32 v[66:67], v[226:227], v[72:73], v[66:67]
	v_pk_fma_f32 v[104:105], v[228:229], v[74:75], v[104:105]
	v_fmac_f32_e32 v66, v76, v234
	v_add_f32_e32 v66, v66, v67
	v_add_f32_e32 v104, v104, v105
	v_add_f32_e32 v77, v66, v104
	ds_read_b128 v[56:59], v128 offset:1664
	ds_read_b128 v[60:63], v128 offset:1680
	ds_read_b128 v[100:103], v128 offset:1696
	ds_read_b128 v[202:205], v128 offset:1712
	s_waitcnt lgkmcnt(10)
	v_fma_f32 v66, v68, v20, v153
	v_fma_f32 v67, v69, v21, 0
	v_pk_fma_f32 v[104:105], v[22:23], v[70:71], 0 op_sel_hi:[1,1,0]
	v_pk_fma_f32 v[66:67], v[24:25], v[72:73], v[66:67]
	v_pk_fma_f32 v[104:105], v[26:27], v[74:75], v[104:105]
	v_pk_fma_f32 v[66:67], v[28:29], v[76:77], v[66:67]
	v_add_f32_e32 v66, v66, v67
	v_add_f32_e32 v104, v104, v105
	v_add_f32_e32 v78, v66, v104
	ds_read_b128 v[226:229], v128 offset:1792
	ds_read_b128 v[234:237], v128 offset:1808
	ds_read_b128 v[20:23], v128 offset:1824
	ds_read_b128 v[24:27], v128 offset:1840
	s_waitcnt lgkmcnt(11)
	v_fma_f32 v66, v68, v32, v154
	v_fma_f32 v67, v69, v33, 0
	v_pk_fma_f32 v[104:105], v[34:35], v[70:71], 0 op_sel_hi:[1,1,0]
	v_pk_fma_f32 v[66:67], v[36:37], v[72:73], v[66:67]
	v_pk_fma_f32 v[104:105], v[38:39], v[74:75], v[104:105]
	v_pk_fma_f32 v[66:67], v[40:41], v[76:77], v[66:67]
	v_fmac_f32_e32 v104, v78, v42
	v_add_f32_e32 v66, v66, v67
	v_add_f32_e32 v104, v104, v105
	v_add_f32_e32 v79, v66, v104
	ds_read_b128 v[28:31], v128 offset:1920
	ds_read_b128 v[32:35], v128 offset:1936
	ds_read_b128 v[36:39], v128 offset:1952
	ds_read_b128 v[40:43], v128 offset:1968
	s_waitcnt lgkmcnt(12)
	v_fma_f32 v66, v68, v44, v155
	v_fma_f32 v67, v69, v45, 0
	v_pk_fma_f32 v[104:105], v[46:47], v[70:71], 0 op_sel_hi:[1,1,0]
	v_pk_fma_f32 v[66:67], v[48:49], v[72:73], v[66:67]
	v_pk_fma_f32 v[104:105], v[50:51], v[74:75], v[104:105]
	v_pk_fma_f32 v[66:67], v[52:53], v[76:77], v[66:67]
	v_pk_fma_f32 v[104:105], v[54:55], v[78:79], v[104:105]
	v_add_f32_e32 v66, v66, v67
	v_add_f32_e32 v104, v104, v105
	v_add_f32_e32 v80, v66, v104
	s_waitcnt lgkmcnt(8)
	v_fma_f32 v66, v68, v56, v156
	v_fma_f32 v67, v69, v57, 0
	v_pk_fma_f32 v[104:105], v[58:59], v[70:71], 0 op_sel_hi:[1,1,0]
	v_pk_fma_f32 v[66:67], v[60:61], v[72:73], v[66:67]
	v_pk_fma_f32 v[104:105], v[62:63], v[74:75], v[104:105]
	v_pk_fma_f32 v[66:67], v[100:101], v[76:77], v[66:67]
	v_pk_fma_f32 v[104:105], v[102:103], v[78:79], v[104:105]
	v_fmac_f32_e32 v66, v80, v202
	v_add_f32_e32 v66, v66, v67
	v_add_f32_e32 v104, v104, v105
	v_add_f32_e32 v81, v66, v104
	ds_read_b128 v[44:47], v128 offset:2048
	ds_read_b128 v[48:51], v128 offset:2064
	ds_read_b128 v[52:55], v128 offset:2080
	ds_read_b128 v[56:59], v128 offset:2096
	s_waitcnt lgkmcnt(8)
; #define LAS __attribute__((address_space(3)))
; DI void phase_scan_a(Frame& F, int l, int u_lo, int u_hi, int u_step) {
;     ...
;             for (int i = 0; i < 32; ++i) { float a0 = (i == cc) ? 1.f : 0.f, a1 = 0.f, a2 = 0.f, a3 = 0.f;
;                 if (i + 1 < 32 && i >= 1) {
; #pragma unroll
;                     for (int q = 0; q < (i + 1 + 3) / 4; ++q) rq[(i + 1) & 1][q] = *(const LAS f32x4*)(AD + (i + 1) * 32 + 4 * q); }
;                 __builtin_amdgcn_sched_barrier(0);
; #pragma unroll
;                 for (int q = 0; q < (i + 3) / 4; ++q) { const f32x4 a = rq[i & 1][q];
;                     if (4 * q + 0 < i) a0 += a[0] * Tc[4 * q + 0]; if (4 * q + 1 < i) a1 += a[1] * Tc[4 * q + 1]; if (4 * q + 2 < i) a2 += a[2] * Tc[4 * q + 2]; if (4 * q + 3 < i) a3 += a[3] * Tc[4 * q + 3]; }
;                 Tc[i] = (a0 + a1) + (a2 + a3);
;                 __builtin_amdgcn_sched_barrier(0); }
	v_fma_f32 v66, v68, v226, v157
	v_fma_f32 v67, v69, v227, 0
	v_pk_fma_f32 v[104:105], v[228:229], v[70:71], 0 op_sel_hi:[1,1,0]
	v_pk_fma_f32 v[66:67], v[234:235], v[72:73], v[66:67]
	v_pk_fma_f32 v[104:105], v[236:237], v[74:75], v[104:105]
	v_pk_fma_f32 v[66:67], v[20:21], v[76:77], v[66:67]
	v_pk_fma_f32 v[104:105], v[22:23], v[78:79], v[104:105]
	v_pk_fma_f32 v[66:67], v[24:25], v[80:81], v[66:67]
	v_add_f32_e32 v66, v66, v67
	v_add_f32_e32 v104, v104, v105
	v_add_f32_e32 v82, v66, v104
	ds_read_b128 v[60:63], v128 offset:2176
	ds_read_b128 v[100:103], v128 offset:2192
	ds_read_b128 v[202:205], v128 offset:2208
	ds_read_b128 v[226:229], v128 offset:2224
	ds_read_b128 v[234:237], v128 offset:2240
	s_waitcnt lgkmcnt(9)
	v_fma_f32 v66, v68, v28, v158
	v_fma_f32 v67, v69, v29, 0
	v_pk_fma_f32 v[104:105], v[30:31], v[70:71], 0 op_sel_hi:[1,1,0]
	v_pk_fma_f32 v[66:67], v[32:33], v[72:73], v[66:67]
	v_pk_fma_f32 v[104:105], v[34:35], v[74:75], v[104:105]
	v_pk_fma_f32 v[66:67], v[36:37], v[76:77], v[66:67]
	v_pk_fma_f32 v[104:105], v[38:39], v[78:79], v[104:105]
	v_pk_fma_f32 v[66:67], v[40:41], v[80:81], v[66:67]
	v_fmac_f32_e32 v104, v82, v42
	v_add_f32_e32 v66, v66, v67
	v_add_f32_e32 v104, v104, v105
	v_add_f32_e32 v83, v66, v104
	ds_read_b128 v[20:23], v128 offset:2304
	ds_read_b128 v[24:27], v128 offset:2320
	ds_read_b128 v[28:31], v128 offset:2336
	ds_read_b128 v[32:35], v128 offset:2352
	ds_read_b128 v[36:39], v128 offset:2368
	s_waitcnt lgkmcnt(10)
	v_fma_f32 v66, v68, v44, v159
	v_fma_f32 v67, v69, v45, 0
	v_pk_fma_f32 v[104:105], v[46:47], v[70:71], 0 op_sel_hi:[1,1,0]
	v_pk_fma_f32 v[66:67], v[48:49], v[72:73], v[66:67]
	v_pk_fma_f32 v[104:105], v[50:51], v[74:75], v[104:105]
	v_pk_fma_f32 v[66:67], v[52:53], v[76:77], v[66:67]
	v_pk_fma_f32 v[104:105], v[54:55], v[78:79], v[104:105]
	v_pk_fma_f32 v[66:67], v[56:57], v[80:81], v[66:67]
	v_pk_fma_f32 v[104:105], v[58:59], v[82:83], v[104:105]
	v_add_f32_e32 v66, v66, v67
	v_add_f32_e32 v104, v104, v105
	v_add_f32_e32 v84, v66, v104
	ds_read_b128 v[40:43], v128 offset:2432
	ds_read_b128 v[44:47], v128 offset:2448
	ds_read_b128 v[48:51], v128 offset:2464
	ds_read_b128 v[52:55], v128 offset:2480
	ds_read_b128 v[56:59], v128 offset:2496
	s_waitcnt lgkmcnt(10)
	v_fma_f32 v66, v68, v60, v160
	v_fma_f32 v67, v69, v61, 0
	v_pk_fma_f32 v[104:105], v[62:63], v[70:71], 0 op_sel_hi:[1,1,0]
	v_pk_fma_f32 v[66:67], v[100:101], v[72:73], v[66:67]
	v_pk_fma_f32 v[104:105], v[102:103], v[74:75], v[104:105]
	v_pk_fma_f32 v[66:67], v[202:203], v[76:77], v[66:67]
	v_pk_fma_f32 v[104:105], v[204:205], v[78:79], v[104:105]
	v_pk_fma_f32 v[66:67], v[226:227], v[80:81], v[66:67]
	v_pk_fma_f32 v[104:105], v[228:229], v[82:83], v[104:105]
	v_fmac_f32_e32 v66, v84, v234
	v_add_f32_e32 v66, v66, v67
	v_add_f32_e32 v104, v104, v105
	v_add_f32_e32 v85, v66, v104
	ds_read_b128 v[60:63], v128 offset:2560
	ds_read_b128 v[100:103], v128 offset:2576
	ds_read_b128 v[202:205], v128 offset:2592
	ds_read_b128 v[226:229], v128 offset:2608
	ds_read_b128 v[234:237], v128 offset:2624
	s_waitcnt lgkmcnt(10)
	v_fma_f32 v66, v68, v20, v161
	v_fma_f32 v67, v69, v21, 0
	v_pk_fma_f32 v[104:105], v[22:23], v[70:71], 0 op_sel_hi:[1,1,0]
	v_pk_fma_f32 v[66:67], v[24:25], v[72:73], v[66:67]
	v_pk_fma_f32 v[104:105], v[26:27], v[74:75], v[104:105]
	v_pk_fma_f32 v[66:67], v[28:29], v[76:77], v[66:67]
	v_pk_fma_f32 v[104:105], v[30:31], v[78:79], v[104:105]
	v_pk_fma_f32 v[66:67], v[32:33], v[80:81], v[66:67]
	v_pk_fma_f32 v[104:105], v[34:35], v[82:83], v[104:105]
	v_pk_fma_f32 v[66:67], v[36:37], v[84:85], v[66:67]
	v_add_f32_e32 v66, v66, v67
	v_add_f32_e32 v104, v104, v105
	v_add_f32_e32 v86, v66, v104
	s_waitcnt lgkmcnt(5)
	v_fma_f32 v66, v68, v40, v162
	v_fma_f32 v67, v69, v41, 0
	v_pk_fma_f32 v[104:105], v[42:43], v[70:71], 0 op_sel_hi:[1,1,0]
	v_pk_fma_f32 v[66:67], v[44:45], v[72:73], v[66:67]
	v_pk_fma_f32 v[104:105], v[46:47], v[74:75], v[104:105]
	v_pk_fma_f32 v[66:67], v[48:49], v[76:77], v[66:67]
	v_pk_fma_f32 v[104:105], v[50:51], v[78:79], v[104:105]
	v_pk_fma_f32 v[66:67], v[52:53], v[80:81], v[66:67]
	v_pk_fma_f32 v[104:105], v[54:55], v[82:83], v[104:105]
	v_pk_fma_f32 v[66:67], v[56:57], v[84:85], v[66:67]
	v_fmac_f32_e32 v104, v86, v58
	v_add_f32_e32 v66, v66, v67
	v_add_f32_e32 v104, v104, v105
	v_add_f32_e32 v87, v66, v104
	ds_read_b128 v[20:23], v128 offset:2688
	ds_read_b128 v[24:27], v128 offset:2704
	ds_read_b128 v[28:31], v128 offset:2720
	ds_read_b128 v[32:35], v128 offset:2736
	ds_read_b128 v[36:39], v128 offset:2752
	ds_read_b128 v[40:43], v128 offset:2768
	s_waitcnt lgkmcnt(6)
	v_fma_f32 v66, v68, v60, v163
	v_fma_f32 v67, v69, v61, 0
	v_pk_fma_f32 v[104:105], v[62:63], v[70:71], 0 op_sel_hi:[1,1,0]
	v_pk_fma_f32 v[66:67], v[100:101], v[72:73], v[66:67]
	v_pk_fma_f32 v[104:105], v[102:103], v[74:75], v[104:105]
	v_pk_fma_f32 v[66:67], v[202:203], v[76:77], v[66:67]
	v_pk_fma_f32 v[104:105], v[204:205], v[78:79], v[104:105]
	v_pk_fma_f32 v[66:67], v[226:227], v[80:81], v[66:67]
	v_pk_fma_f32 v[104:105], v[228:229], v[82:83], v[104:105]
	v_pk_fma_f32 v[66:67], v[234:235], v[84:85], v[66:67]
	v_pk_fma_f32 v[104:105], v[236:237], v[86:87], v[104:105]
	v_add_f32_e32 v66, v66, v67
	v_add_f32_e32 v104, v104, v105
	v_add_f32_e32 v88, v66, v104
	ds_read_b128 v[44:47], v128 offset:2816
	ds_read_b128 v[48:51], v128 offset:2832
	ds_read_b128 v[52:55], v128 offset:2848
	ds_read_b128 v[56:59], v128 offset:2864
	ds_read_b128 v[60:63], v128 offset:2880
	ds_read_b128 v[100:103], v128 offset:2896
	s_waitcnt lgkmcnt(6)
; #define LAS __attribute__((address_space(3)))
; DI void phase_scan_a(Frame& F, int l, int u_lo, int u_hi, int u_step) {
;     ...
;             for (int i = 0; i < 32; ++i) { float a0 = (i == cc) ? 1.f : 0.f, a1 = 0.f, a2 = 0.f, a3 = 0.f;
;                 if (i + 1 < 32 && i >= 1) {
; #pragma unroll
;                     for (int q = 0; q < (i + 1 + 3) / 4; ++q) rq[(i + 1) & 1][q] = *(const LAS f32x4*)(AD + (i + 1) * 32 + 4 * q); }
;                 __builtin_amdgcn_sched_barrier(0);
; #pragma unroll
;                 for (int q = 0; q < (i + 3) / 4; ++q) { const f32x4 a = rq[i & 1][q];
;                     if (4 * q + 0 < i) a0 += a[0] * Tc[4 * q + 0]; if (4 * q + 1 < i) a1 += a[1] * Tc[4 * q + 1]; if (4 * q + 2 < i) a2 += a[2] * Tc[4 * q + 2]; if (4 * q + 3 < i) a3 += a[3] * Tc[4 * q + 3]; }
;                 Tc[i] = (a0 + a1) + (a2 + a3);
;                 __builtin_amdgcn_sched_barrier(0); }
	v_fma_f32 v66, v68, v20, v164
	v_fma_f32 v67, v69, v21, 0
	v_pk_fma_f32 v[104:105], v[22:23], v[70:71], 0 op_sel_hi:[1,1,0]
	v_pk_fma_f32 v[66:67], v[24:25], v[72:73], v[66:67]
	v_pk_fma_f32 v[104:105], v[26:27], v[74:75], v[104:105]
	v_pk_fma_f32 v[66:67], v[28:29], v[76:77], v[66:67]
	v_pk_fma_f32 v[104:105], v[30:31], v[78:79], v[104:105]
	v_pk_fma_f32 v[66:67], v[32:33], v[80:81], v[66:67]
	v_pk_fma_f32 v[104:105], v[34:35], v[82:83], v[104:105]
	v_pk_fma_f32 v[66:67], v[36:37], v[84:85], v[66:67]
	v_pk_fma_f32 v[104:105], v[38:39], v[86:87], v[104:105]
	v_fmac_f32_e32 v66, v88, v40
	v_add_f32_e32 v66, v66, v67
	v_add_f32_e32 v104, v104, v105
	v_add_f32_e32 v89, v66, v104
	ds_read_b128 v[202:205], v128 offset:2944
	ds_read_b128 v[226:229], v128 offset:2960
	ds_read_b128 v[234:237], v128 offset:2976
	ds_read_b128 v[20:23], v128 offset:2992
	ds_read_b128 v[24:27], v128 offset:3008
	ds_read_b128 v[28:31], v128 offset:3024
	s_waitcnt lgkmcnt(6)
	v_fma_f32 v66, v68, v44, v165
	v_fma_f32 v67, v69, v45, 0
	v_pk_fma_f32 v[104:105], v[46:47], v[70:71], 0 op_sel_hi:[1,1,0]
	v_pk_fma_f32 v[66:67], v[48:49], v[72:73], v[66:67]
	v_pk_fma_f32 v[104:105], v[50:51], v[74:75], v[104:105]
	v_pk_fma_f32 v[66:67], v[52:53], v[76:77], v[66:67]
	v_pk_fma_f32 v[104:105], v[54:55], v[78:79], v[104:105]
	v_pk_fma_f32 v[66:67], v[56:57], v[80:81], v[66:67]
	v_pk_fma_f32 v[104:105], v[58:59], v[82:83], v[104:105]
	v_pk_fma_f32 v[66:67], v[60:61], v[84:85], v[66:67]
	v_pk_fma_f32 v[104:105], v[62:63], v[86:87], v[104:105]
	v_pk_fma_f32 v[66:67], v[100:101], v[88:89], v[66:67]
	v_add_f32_e32 v66, v66, v67
	v_add_f32_e32 v104, v104, v105
	v_add_f32_e32 v90, v66, v104
	ds_read_b128 v[32:35], v128 offset:3072
	ds_read_b128 v[36:39], v128 offset:3088
	ds_read_b128 v[40:43], v128 offset:3104
	ds_read_b128 v[44:47], v128 offset:3120
	ds_read_b128 v[48:51], v128 offset:3136
	ds_read_b128 v[52:55], v128 offset:3152
	s_waitcnt lgkmcnt(6)
	v_fma_f32 v66, v68, v202, v166
	v_fma_f32 v67, v69, v203, 0
	v_pk_fma_f32 v[104:105], v[204:205], v[70:71], 0 op_sel_hi:[1,1,0]
	v_pk_fma_f32 v[66:67], v[226:227], v[72:73], v[66:67]
	v_pk_fma_f32 v[104:105], v[228:229], v[74:75], v[104:105]
	v_pk_fma_f32 v[66:67], v[234:235], v[76:77], v[66:67]
	v_pk_fma_f32 v[104:105], v[236:237], v[78:79], v[104:105]
	v_pk_fma_f32 v[66:67], v[20:21], v[80:81], v[66:67]
	v_pk_fma_f32 v[104:105], v[22:23], v[82:83], v[104:105]
	v_pk_fma_f32 v[66:67], v[24:25], v[84:85], v[66:67]
	v_pk_fma_f32 v[104:105], v[26:27], v[86:87], v[104:105]
	v_pk_fma_f32 v[66:67], v[28:29], v[88:89], v[66:67]
	v_fmac_f32_e32 v104, v90, v30
	v_add_f32_e32 v66, v66, v67
	v_add_f32_e32 v104, v104, v105
	v_add_f32_e32 v91, v66, v104
	ds_read_b128 v[56:59], v128 offset:3200
	ds_read_b128 v[60:63], v128 offset:3216
	ds_read_b128 v[100:103], v128 offset:3232
	ds_read_b128 v[202:205], v128 offset:3248
	ds_read_b128 v[226:229], v128 offset:3264
	ds_read_b128 v[234:237], v128 offset:3280
	ds_read_b128 v[20:23], v128 offset:3296
	s_waitcnt lgkmcnt(7)
	v_fma_f32 v66, v68, v32, v167
	v_fma_f32 v67, v69, v33, 0
	v_pk_fma_f32 v[104:105], v[34:35], v[70:71], 0 op_sel_hi:[1,1,0]
	v_pk_fma_f32 v[66:67], v[36:37], v[72:73], v[66:67]
	v_pk_fma_f32 v[104:105], v[38:39], v[74:75], v[104:105]
	v_pk_fma_f32 v[66:67], v[40:41], v[76:77], v[66:67]
	v_pk_fma_f32 v[104:105], v[42:43], v[78:79], v[104:105]
	v_pk_fma_f32 v[66:67], v[44:45], v[80:81], v[66:67]
	v_pk_fma_f32 v[104:105], v[46:47], v[82:83], v[104:105]
	v_pk_fma_f32 v[66:67], v[48:49], v[84:85], v[66:67]
	v_pk_fma_f32 v[104:105], v[50:51], v[86:87], v[104:105]
	v_pk_fma_f32 v[66:67], v[52:53], v[88:89], v[66:67]
	v_pk_fma_f32 v[104:105], v[54:55], v[90:91], v[104:105]
	v_add_f32_e32 v66, v66, v67
	v_add_f32_e32 v104, v104, v105
	v_add_f32_e32 v92, v66, v104
	ds_read_b128 v[24:27], v128 offset:3328
	ds_read_b128 v[28:31], v128 offset:3344
	ds_read_b128 v[32:35], v128 offset:3360
	ds_read_b128 v[36:39], v128 offset:3376
	ds_read_b128 v[40:43], v128 offset:3392
	ds_read_b128 v[44:47], v128 offset:3408
	ds_read_b128 v[48:51], v128 offset:3424
	s_waitcnt lgkmcnt(7)
	v_fma_f32 v66, v68, v56, v168
	v_fma_f32 v67, v69, v57, 0
	v_pk_fma_f32 v[104:105], v[58:59], v[70:71], 0 op_sel_hi:[1,1,0]
	v_pk_fma_f32 v[66:67], v[60:61], v[72:73], v[66:67]
	v_pk_fma_f32 v[104:105], v[62:63], v[74:75], v[104:105]
	v_pk_fma_f32 v[66:67], v[100:101], v[76:77], v[66:67]
	v_pk_fma_f32 v[104:105], v[102:103], v[78:79], v[104:105]
	v_pk_fma_f32 v[66:67], v[202:203], v[80:81], v[66:67]
	v_pk_fma_f32 v[104:105], v[204:205], v[82:83], v[104:105]
	v_pk_fma_f32 v[66:67], v[226:227], v[84:85], v[66:67]
	v_pk_fma_f32 v[104:105], v[228:229], v[86:87], v[104:105]
	v_pk_fma_f32 v[66:67], v[234:235], v[88:89], v[66:67]
	v_pk_fma_f32 v[104:105], v[236:237], v[90:91], v[104:105]
	v_fmac_f32_e32 v66, v92, v20
	v_add_f32_e32 v66, v66, v67
	v_add_f32_e32 v104, v104, v105
	v_add_f32_e32 v93, v66, v104
	ds_read_b128 v[52:55], v128 offset:3456
	ds_read_b128 v[56:59], v128 offset:3472
	ds_read_b128 v[60:63], v128 offset:3488
	ds_read_b128 v[100:103], v128 offset:3504
	ds_read_b128 v[202:205], v128 offset:3520
	ds_read_b128 v[226:229], v128 offset:3536
	ds_read_b128 v[234:237], v128 offset:3552
	s_waitcnt lgkmcnt(7)
; #define LAS __attribute__((address_space(3)))
; DI void phase_scan_a(Frame& F, int l, int u_lo, int u_hi, int u_step) {
;     ...
;             for (int i = 0; i < 32; ++i) { float a0 = (i == cc) ? 1.f : 0.f, a1 = 0.f, a2 = 0.f, a3 = 0.f;
;                 if (i + 1 < 32 && i >= 1) {
; #pragma unroll
;                     for (int q = 0; q < (i + 1 + 3) / 4; ++q) rq[(i + 1) & 1][q] = *(const LAS f32x4*)(AD + (i + 1) * 32 + 4 * q); }
;                 __builtin_amdgcn_sched_barrier(0);
; #pragma unroll
;                 for (int q = 0; q < (i + 3) / 4; ++q) { const f32x4 a = rq[i & 1][q];
;                     if (4 * q + 0 < i) a0 += a[0] * Tc[4 * q + 0]; if (4 * q + 1 < i) a1 += a[1] * Tc[4 * q + 1]; if (4 * q + 2 < i) a2 += a[2] * Tc[4 * q + 2]; if (4 * q + 3 < i) a3 += a[3] * Tc[4 * q + 3]; }
;                 Tc[i] = (a0 + a1) + (a2 + a3);
;                 __builtin_amdgcn_sched_barrier(0); }
	v_fma_f32 v66, v68, v24, v169
	v_fma_f32 v67, v69, v25, 0
	v_pk_fma_f32 v[104:105], v[26:27], v[70:71], 0 op_sel_hi:[1,1,0]
	v_pk_fma_f32 v[66:67], v[28:29], v[72:73], v[66:67]
	v_pk_fma_f32 v[104:105], v[30:31], v[74:75], v[104:105]
	v_pk_fma_f32 v[66:67], v[32:33], v[76:77], v[66:67]
	v_pk_fma_f32 v[104:105], v[34:35], v[78:79], v[104:105]
	v_pk_fma_f32 v[66:67], v[36:37], v[80:81], v[66:67]
	v_pk_fma_f32 v[104:105], v[38:39], v[82:83], v[104:105]
	v_pk_fma_f32 v[66:67], v[40:41], v[84:85], v[66:67]
	v_pk_fma_f32 v[104:105], v[42:43], v[86:87], v[104:105]
	v_pk_fma_f32 v[66:67], v[44:45], v[88:89], v[66:67]
	v_pk_fma_f32 v[104:105], v[46:47], v[90:91], v[104:105]
	v_pk_fma_f32 v[66:67], v[48:49], v[92:93], v[66:67]
	v_add_f32_e32 v66, v66, v67
	v_add_f32_e32 v104, v104, v105
	v_add_f32_e32 v94, v66, v104
	ds_read_b128 v[20:23], v128 offset:3584
	ds_read_b128 v[24:27], v128 offset:3600
	ds_read_b128 v[28:31], v128 offset:3616
	ds_read_b128 v[32:35], v128 offset:3632
	ds_read_b128 v[36:39], v128 offset:3648
	ds_read_b128 v[40:43], v128 offset:3664
	ds_read_b128 v[44:47], v128 offset:3680
	s_waitcnt lgkmcnt(7)
	v_fma_f32 v66, v68, v52, v170
	v_fma_f32 v67, v69, v53, 0
	v_pk_fma_f32 v[104:105], v[54:55], v[70:71], 0 op_sel_hi:[1,1,0]
	v_pk_fma_f32 v[66:67], v[56:57], v[72:73], v[66:67]
	v_pk_fma_f32 v[104:105], v[58:59], v[74:75], v[104:105]
	v_pk_fma_f32 v[66:67], v[60:61], v[76:77], v[66:67]
	v_pk_fma_f32 v[104:105], v[62:63], v[78:79], v[104:105]
	v_pk_fma_f32 v[66:67], v[100:101], v[80:81], v[66:67]
	v_pk_fma_f32 v[104:105], v[102:103], v[82:83], v[104:105]
	v_pk_fma_f32 v[66:67], v[202:203], v[84:85], v[66:67]
	v_pk_fma_f32 v[104:105], v[204:205], v[86:87], v[104:105]
	v_pk_fma_f32 v[66:67], v[226:227], v[88:89], v[66:67]
	v_pk_fma_f32 v[104:105], v[228:229], v[90:91], v[104:105]
	v_pk_fma_f32 v[66:67], v[234:235], v[92:93], v[66:67]
	v_fmac_f32_e32 v104, v94, v236
	v_add_f32_e32 v66, v66, v67
	v_add_f32_e32 v104, v104, v105
	v_add_f32_e32 v95, v66, v104
	ds_read_b128 v[48:51], v128 offset:3712
	ds_read_b128 v[52:55], v128 offset:3728
	ds_read_b128 v[56:59], v128 offset:3744
	ds_read_b128 v[60:63], v128 offset:3760
	ds_read_b128 v[100:103], v128 offset:3776
	ds_read_b128 v[202:205], v128 offset:3792
	ds_read_b128 v[226:229], v128 offset:3808
	ds_read_b128 v[234:237], v128 offset:3824
	s_waitcnt lgkmcnt(8)
	v_fma_f32 v66, v68, v20, v171
	v_fma_f32 v67, v69, v21, 0
	v_pk_fma_f32 v[104:105], v[22:23], v[70:71], 0 op_sel_hi:[1,1,0]
	v_pk_fma_f32 v[66:67], v[24:25], v[72:73], v[66:67]
	v_pk_fma_f32 v[104:105], v[26:27], v[74:75], v[104:105]
	v_pk_fma_f32 v[66:67], v[28:29], v[76:77], v[66:67]
	v_pk_fma_f32 v[104:105], v[30:31], v[78:79], v[104:105]
	v_pk_fma_f32 v[66:67], v[32:33], v[80:81], v[66:67]
	v_pk_fma_f32 v[104:105], v[34:35], v[82:83], v[104:105]
	v_pk_fma_f32 v[66:67], v[36:37], v[84:85], v[66:67]
	v_pk_fma_f32 v[104:105], v[38:39], v[86:87], v[104:105]
	v_pk_fma_f32 v[66:67], v[40:41], v[88:89], v[66:67]
	v_pk_fma_f32 v[104:105], v[42:43], v[90:91], v[104:105]
	v_pk_fma_f32 v[66:67], v[44:45], v[92:93], v[66:67]
	v_pk_fma_f32 v[104:105], v[46:47], v[94:95], v[104:105]
	v_add_f32_e32 v66, v66, v67
	v_add_f32_e32 v104, v104, v105
	v_add_f32_e32 v96, v66, v104
	s_waitcnt lgkmcnt(0)
	v_fma_f32 v66, v68, v48, v172
	v_fma_f32 v67, v69, v49, 0
	v_pk_fma_f32 v[104:105], v[50:51], v[70:71], 0 op_sel_hi:[1,1,0]
	v_pk_fma_f32 v[66:67], v[52:53], v[72:73], v[66:67]
	v_pk_fma_f32 v[104:105], v[54:55], v[74:75], v[104:105]
	v_pk_fma_f32 v[66:67], v[56:57], v[76:77], v[66:67]
	v_pk_fma_f32 v[104:105], v[58:59], v[78:79], v[104:105]
	v_pk_fma_f32 v[66:67], v[60:61], v[80:81], v[66:67]
	v_pk_fma_f32 v[104:105], v[62:63], v[82:83], v[104:105]
	v_pk_fma_f32 v[66:67], v[100:101], v[84:85], v[66:67]
	v_pk_fma_f32 v[104:105], v[102:103], v[86:87], v[104:105]
	v_pk_fma_f32 v[66:67], v[202:203], v[88:89], v[66:67]
	v_pk_fma_f32 v[104:105], v[204:205], v[90:91], v[104:105]
	v_pk_fma_f32 v[66:67], v[226:227], v[92:93], v[66:67]
	v_pk_fma_f32 v[104:105], v[228:229], v[94:95], v[104:105]
	v_fmac_f32_e32 v66, v96, v234
	v_add_f32_e32 v66, v66, v67
	v_add_f32_e32 v104, v104, v105
	v_add_f32_e32 v97, v66, v104
	ds_read_b128 v[20:23], v128 offset:3840
	ds_read_b128 v[24:27], v128 offset:3856
	ds_read_b128 v[28:31], v128 offset:3872
	ds_read_b128 v[32:35], v128 offset:3888
	ds_read_b128 v[36:39], v128 offset:3904
	ds_read_b128 v[40:43], v128 offset:3920
	ds_read_b128 v[44:47], v128 offset:3936
	ds_read_b128 v[48:51], v128 offset:3952
	s_waitcnt lgkmcnt(0)
; #define LAS __attribute__((address_space(3)))
; DI unsigned pk2(float lo, float hi) { f32x2 v = {lo, hi}; return __builtin_bit_cast(unsigned, __builtin_convertvector(v, bf16v2)); }
; DI bf16_t f2bf(float f) { return (bf16_t)(pk2(f, 0.f) & 0xffffu); }
; DI void phase_scan_a(Frame& F, int l, int u_lo, int u_hi, int u_step) {
;     ...
;             for (int i = 0; i < 32; ++i) { float a0 = (i == cc) ? 1.f : 0.f, a1 = 0.f, a2 = 0.f, a3 = 0.f;
;                 if (i + 1 < 32 && i >= 1) {
; #pragma unroll
;                     for (int q = 0; q < (i + 1 + 3) / 4; ++q) rq[(i + 1) & 1][q] = *(const LAS f32x4*)(AD + (i + 1) * 32 + 4 * q); }
;                 __builtin_amdgcn_sched_barrier(0);
; #pragma unroll
;                 for (int q = 0; q < (i + 3) / 4; ++q) { const f32x4 a = rq[i & 1][q];
;                     if (4 * q + 0 < i) a0 += a[0] * Tc[4 * q + 0]; if (4 * q + 1 < i) a1 += a[1] * Tc[4 * q + 1]; if (4 * q + 2 < i) a2 += a[2] * Tc[4 * q + 2]; if (4 * q + 3 < i) a3 += a[3] * Tc[4 * q + 3]; }
;                 Tc[i] = (a0 + a1) + (a2 + a3);
;                 __builtin_amdgcn_sched_barrier(0); }
; #pragma unroll
;             for (int i = 0; i < 32; ++i) *(LAS bf16_t*)(MB(11) + (32 * blk + i) * MP + (32 * blk + cc) * 2) = f2bf(Tc[i]);
;             if (blk == 0) {
; #pragma unroll
;                 for (int q = 0; q < 4; ++q) { u32x4 w; w.x = pk2(Tc[8 * q], Tc[8 * q + 1]); w.y = pk2(Tc[8 * q + 2], Tc[8 * q + 3]); w.z = pk2(Tc[8 * q + 4], Tc[8 * q + 5]); w.w = pk2(Tc[8 * q + 6], Tc[8 * q + 7]);
;                     *(LAS u32x4*)(T11T + cc * SP + q * 16) = w; }
;             } else {
;                 unsigned z = 0u; asm volatile("" : "+v"(z));
; #pragma unroll
;                 for (int q = 0; q < 4; ++q) *(LAS u32x4*)(MB(11) + cc * MP + 64 + q * 16) = (u32x4){z, z, z, z};
	v_fma_f32 v66, v68, v20, v173
	v_fma_f32 v67, v69, v21, 0
	v_pk_fma_f32 v[104:105], v[22:23], v[70:71], 0 op_sel_hi:[1,1,0]
	v_pk_fma_f32 v[66:67], v[24:25], v[72:73], v[66:67]
	v_pk_fma_f32 v[104:105], v[26:27], v[74:75], v[104:105]
	v_pk_fma_f32 v[66:67], v[28:29], v[76:77], v[66:67]
	v_pk_fma_f32 v[104:105], v[30:31], v[78:79], v[104:105]
	v_pk_fma_f32 v[66:67], v[32:33], v[80:81], v[66:67]
	v_pk_fma_f32 v[104:105], v[34:35], v[82:83], v[104:105]
	v_pk_fma_f32 v[66:67], v[36:37], v[84:85], v[66:67]
	v_pk_fma_f32 v[104:105], v[38:39], v[86:87], v[104:105]
	v_pk_fma_f32 v[66:67], v[40:41], v[88:89], v[66:67]
	v_pk_fma_f32 v[104:105], v[42:43], v[90:91], v[104:105]
	v_pk_fma_f32 v[66:67], v[44:45], v[92:93], v[66:67]
	v_pk_fma_f32 v[104:105], v[46:47], v[94:95], v[104:105]
	v_pk_fma_f32 v[66:67], v[48:49], v[96:97], v[66:67]
	v_add_f32_e32 v66, v66, v67
	v_add_f32_e32 v104, v104, v105
	v_add_f32_e32 v98, v66, v104
	ds_read_b128 v[52:55], v128 offset:3968
	ds_read_b128 v[56:59], v128 offset:3984
	ds_read_b128 v[60:63], v128 offset:4000
	ds_read_b128 v[100:103], v128 offset:4016
	ds_read_b128 v[202:205], v128 offset:4032
	ds_read_b128 v[226:229], v128 offset:4048
	ds_read_b128 v[234:237], v128 offset:4064
	ds_read_b128 v[20:23], v128 offset:4080
	s_waitcnt lgkmcnt(0)
	v_fma_f32 v66, v68, v52, v174
	v_fma_f32 v67, v69, v53, 0
	v_pk_fma_f32 v[104:105], v[54:55], v[70:71], 0 op_sel_hi:[1,1,0]
	v_pk_fma_f32 v[66:67], v[56:57], v[72:73], v[66:67]
	v_pk_fma_f32 v[104:105], v[58:59], v[74:75], v[104:105]
	v_pk_fma_f32 v[66:67], v[60:61], v[76:77], v[66:67]
	v_pk_fma_f32 v[104:105], v[62:63], v[78:79], v[104:105]
	v_pk_fma_f32 v[66:67], v[100:101], v[80:81], v[66:67]
	v_pk_fma_f32 v[104:105], v[102:103], v[82:83], v[104:105]
	v_pk_fma_f32 v[66:67], v[202:203], v[84:85], v[66:67]
	v_pk_fma_f32 v[104:105], v[204:205], v[86:87], v[104:105]
	v_pk_fma_f32 v[66:67], v[226:227], v[88:89], v[66:67]
	v_pk_fma_f32 v[104:105], v[228:229], v[90:91], v[104:105]
	v_pk_fma_f32 v[66:67], v[234:235], v[92:93], v[66:67]
	v_pk_fma_f32 v[104:105], v[236:237], v[94:95], v[104:105]
	v_pk_fma_f32 v[66:67], v[20:21], v[96:97], v[66:67]
	v_fmac_f32_e32 v104, v98, v22
	v_add_f32_e32 v66, v66, v67
	v_add_f32_e32 v104, v104, v105
	v_add_f32_e32 v99, v66, v104
	v_cvt_pk_bf16_f32 v21, v69, s0
	ds_write_b16 v195, v21 offset:144
	v_cvt_pk_bf16_f32 v20, v70, s0
	ds_write_b16 v195, v20 offset:288
	v_cvt_pk_bf16_f32 v21, v71, s0
	ds_write_b16 v195, v21 offset:432
	v_cvt_pk_bf16_f32 v20, v72, s0
	ds_write_b16 v195, v20 offset:576
	v_cvt_pk_bf16_f32 v21, v73, s0
	ds_write_b16 v195, v21 offset:720
	v_cvt_pk_bf16_f32 v20, v74, s0
	ds_write_b16 v195, v20 offset:864
	v_cvt_pk_bf16_f32 v21, v75, s0
	ds_write_b16 v195, v21 offset:1008
	v_cvt_pk_bf16_f32 v20, v76, s0
	ds_write_b16 v195, v20 offset:1152
	v_cvt_pk_bf16_f32 v21, v77, s0
	ds_write_b16 v195, v21 offset:1296
	v_cvt_pk_bf16_f32 v20, v78, s0
	ds_write_b16 v195, v20 offset:1440
	v_cvt_pk_bf16_f32 v21, v79, s0
	ds_write_b16 v195, v21 offset:1584
	v_cvt_pk_bf16_f32 v20, v80, s0
	ds_write_b16 v195, v20 offset:1728
	v_cvt_pk_bf16_f32 v21, v81, s0
	ds_write_b16 v195, v21 offset:1872
	v_cvt_pk_bf16_f32 v20, v82, s0
	ds_write_b16 v195, v20 offset:2016
	v_cvt_pk_bf16_f32 v21, v83, s0
	ds_write_b16 v195, v21 offset:2160
	v_cvt_pk_bf16_f32 v20, v84, s0
	ds_write_b16 v195, v20 offset:2304
	v_cvt_pk_bf16_f32 v21, v85, s0
	ds_write_b16 v195, v21 offset:2448
	v_cvt_pk_bf16_f32 v20, v86, s0
	ds_write_b16 v195, v20 offset:2592
	v_cvt_pk_bf16_f32 v21, v87, s0
	ds_write_b16 v195, v21 offset:2736
	v_cvt_pk_bf16_f32 v20, v88, s0
	ds_write_b16 v195, v20 offset:2880
	v_cvt_pk_bf16_f32 v21, v89, s0
	ds_write_b16 v195, v21 offset:3024
	v_cvt_pk_bf16_f32 v20, v90, s0
	ds_write_b16 v195, v20 offset:3168
	v_cvt_pk_bf16_f32 v21, v91, s0
	ds_write_b16 v195, v21 offset:3312
	v_cvt_pk_bf16_f32 v20, v92, s0
	ds_write_b16 v195, v20 offset:3456
	v_cvt_pk_bf16_f32 v21, v93, s0
	ds_write_b16 v195, v21 offset:3600
	v_cvt_pk_bf16_f32 v20, v94, s0
	ds_write_b16 v195, v20 offset:3744
	v_cvt_pk_bf16_f32 v21, v95, s0
	ds_write_b16 v195, v21 offset:3888
	v_cvt_pk_bf16_f32 v20, v96, s0
	ds_write_b16 v195, v20 offset:4032
	v_cvt_pk_bf16_f32 v21, v97, s0
	ds_write_b16 v195, v21 offset:4176
	v_cvt_pk_bf16_f32 v20, v98, s0
	ds_write_b16 v195, v20 offset:4320
	v_cvt_pk_bf16_f32 v21, v99, s0
	ds_write_b16 v195, v180
	ds_write_b16 v196, v21
	s_mov_b64 s[40:41], exec
	v_readlane_b32 s42, v254, 24
	v_readlane_b32 s43, v254, 25
	s_and_b64 s[42:43], s[40:41], s[42:43]
	s_xor_b64 s[40:41], s[42:43], s[40:41]
	s_mov_b64 exec, s[42:43]
	s_cbranch_execz .LBB0_1135
	v_mov_b32_e32 v20, v65
	s_nop 0
	v_mov_b32_e32 v21, v20
	v_mov_b32_e32 v22, v20
	v_mov_b32_e32 v23, v20
	ds_write_b128 v129, v[20:23]
	ds_write_b128 v181, v[20:23]
	ds_write_b128 v182, v[20:23]
	ds_write_b128 v183, v[20:23]
.LBB0_1135:
	s_andn2_saveexec_b64 s[40:41], s[40:41]
	s_cbranch_execz .LBB0_1137
	v_cvt_pk_bf16_f32 v20, v68, v69
	v_cvt_pk_bf16_f32 v21, v70, v71
	v_cvt_pk_bf16_f32 v22, v72, v73
	v_cvt_pk_bf16_f32 v23, v74, v75
	ds_write_b128 v197, v[20:23]
	v_cvt_pk_bf16_f32 v20, v76, v77
	v_cvt_pk_bf16_f32 v21, v78, v79
	v_cvt_pk_bf16_f32 v22, v80, v81
	v_cvt_pk_bf16_f32 v23, v82, v83
	ds_write_b128 v197, v[20:23] offset:16
	v_cvt_pk_bf16_f32 v20, v84, v85
	v_cvt_pk_bf16_f32 v21, v86, v87
	v_cvt_pk_bf16_f32 v22, v88, v89
	v_cvt_pk_bf16_f32 v23, v90, v91
	ds_write_b128 v197, v[20:23] offset:32
	v_cvt_pk_bf16_f32 v20, v92, v93
	v_cvt_pk_bf16_f32 v21, v94, v95
	v_cvt_pk_bf16_f32 v22, v96, v97
	v_cvt_pk_bf16_f32 v23, v98, v99
	ds_write_b128 v197, v[20:23] offset:48

; #define LAS __attribute__((address_space(3)))
;     ...
;                 bf16x8 ka[2][4];
; #pragma unroll
;                 for (int k2 = 0; k2 < 2; ++k2)
; #pragma unroll
;                     for (int kk = 0; kk < 4; ++kk) ka[k2][kk] = *(const LAS bf16x8*)(Ks + (32 * (2 * ck + k2) + qi) * KS_PITCH + (16 * kk + 8 * half) * 2);
;                 f32x16 sacc[2];
; #pragma unroll
;                 for (int k2 = 0; k2 < 2; ++k2) {
; #pragma unroll
;                     for (int i = 0; i < 16; ++i) sacc[k2][i] = 0.f;
; #pragma unroll
;                     for (int kk = 0; kk < 4; ++kk) sacc[k2] = __builtin_amdgcn_mfma_f32_32x32x16_bf16(ka[k2][kk], qf[kk], sacc[k2], 0, 0, 0); }
.LBB0_2230:
	v_mov_b32_e32 v64, v250
	s_waitcnt lgkmcnt(0)
	ds_read_b128 v[32:35], v251
	ds_read_b128 v[66:69], v251 offset:32
	ds_read_b128 v[70:73], v251 offset:64
	ds_read_b128 v[74:77], v251 offset:96
	ds_read_b128 v[78:81], v251 offset:4608
	ds_read_b128 v[122:125], v251 offset:4640
	v_cmp_ge_i32_e32 vcc, s22, v64
	s_waitcnt lgkmcnt(5)
	v_mfma_f32_32x32x16_bf16 v[48:63], v[32:35], v[110:113], 0
	s_waitcnt lgkmcnt(4)
	v_mfma_f32_32x32x16_bf16 v[48:63], v[66:69], v[106:109], v[48:63]
	ds_read_b128 v[66:69], v251 offset:4672
	s_waitcnt lgkmcnt(4)
	v_mfma_f32_32x32x16_bf16 v[48:63], v[70:73], v[102:105], v[48:63]
	ds_read_b128 v[70:73], v251 offset:4704
	s_waitcnt lgkmcnt(4)
	v_mfma_f32_32x32x16_bf16 v[48:63], v[74:77], v[98:101], v[48:63]
	s_waitcnt lgkmcnt(3)
	v_mfma_f32_32x32x16_bf16 v[32:47], v[78:81], v[110:113], 0
	s_waitcnt lgkmcnt(2)
	v_mfma_f32_32x32x16_bf16 v[32:47], v[122:125], v[106:109], v[32:47]
	s_waitcnt lgkmcnt(1)
	v_mfma_f32_32x32x16_bf16 v[32:47], v[66:69], v[102:105], v[32:47]
	s_waitcnt lgkmcnt(0)
	v_mfma_f32_32x32x16_bf16 v[32:47], v[70:73], v[98:101], v[32:47]
	s_cbranch_vccz .LBB0_2237
;     ...
;                 if (__any(qrel <= 64 * ck + 191)) {
; #pragma unroll
;                     for (int k2 = 0; k2 < 2; ++k2) {
;                         float bb[16];
; #pragma unroll
;                         for (int i = 0; i < 16; ++i) { const int key = 32 * (2 * ck + k2) + (i & 3) + 8 * (i >> 2) + 4 * half; const int n = qrel - key;
;                             bb[i] = LUT[1 + (n < -1 ? -1 : (n > 128 ? 128 : n))]; }
; #pragma unroll
;                         for (int i = 0; i < 16; ++i) asm volatile("" : "+v"(bb[i]));
; #pragma unroll
;                         for (int i = 0; i < 16; ++i) { const float s = sacc[k2][i] + bb[i]; sacc[k2][i] = s; mx = fmaxf(mx, s); } }
	v_add3_u32 v64, v155, v64, s21
	v_subrev_u32_e32 v168, 43, v64
	v_add_u32_e32 v123, -1, v64
	v_add_u32_e32 v124, -2, v64
	v_add_u32_e32 v125, -3, v64
	v_add_u32_e32 v126, -8, v64
	v_add_u32_e32 v127, -9, v64
	v_add_u32_e32 v128, -10, v64
	v_add_u32_e32 v129, -11, v64
	v_add_u32_e32 v130, -16, v64
	v_subrev_u32_e32 v131, 17, v64
	v_subrev_u32_e32 v132, 18, v64
	v_subrev_u32_e32 v133, 19, v64
	v_subrev_u32_e32 v134, 24, v64
	v_subrev_u32_e32 v135, 25, v64
	v_subrev_u32_e32 v136, 26, v64
	v_subrev_u32_e32 v137, 27, v64
	v_med3_i32 v168, v168, -1, v232
	v_med3_i32 v122, v64, -1, v232
	v_med3_i32 v123, v123, -1, v232
	v_med3_i32 v124, v124, -1, v232
	v_med3_i32 v125, v125, -1, v232
	v_med3_i32 v126, v126, -1, v232
	v_med3_i32 v127, v127, -1, v232
	v_med3_i32 v128, v128, -1, v232
	v_med3_i32 v129, v129, -1, v232
	v_med3_i32 v130, v130, -1, v232
	v_med3_i32 v131, v131, -1, v232
	v_med3_i32 v132, v132, -1, v232
	v_med3_i32 v133, v133, -1, v232
	v_med3_i32 v134, v134, -1, v232
	v_med3_i32 v135, v135, -1, v232
	v_med3_i32 v136, v136, -1, v232
	v_med3_i32 v137, v137, -1, v232
	v_lshl_add_u32 v171, v168, 2, s33
	v_subrev_u32_e32 v168, 48, v64
	v_lshl_add_u32 v122, v122, 2, s33
	v_lshl_add_u32 v123, v123, 2, s33
	v_lshl_add_u32 v124, v124, 2, s33
	v_lshl_add_u32 v125, v125, 2, s33
	v_lshl_add_u32 v126, v126, 2, s33
	v_lshl_add_u32 v127, v127, 2, s33
	v_lshl_add_u32 v128, v128, 2, s33
	v_lshl_add_u32 v129, v129, 2, s33
	v_lshl_add_u32 v130, v130, 2, s33
	v_lshl_add_u32 v131, v131, 2, s33
	v_lshl_add_u32 v132, v132, 2, s33
	v_lshl_add_u32 v133, v133, 2, s33
	v_lshl_add_u32 v134, v134, 2, s33
	v_lshl_add_u32 v135, v135, 2, s33
	v_lshl_add_u32 v136, v136, 2, s33
	v_lshl_add_u32 v137, v137, 2, s33
	v_med3_i32 v168, v168, -1, v232
	ds_read_b32 v122, v122 offset:4
	ds_read_b32 v123, v123 offset:4
	ds_read_b32 v124, v124 offset:4
	ds_read_b32 v125, v125 offset:4
	ds_read_b32 v126, v126 offset:4
	ds_read_b32 v127, v127 offset:4
	ds_read_b32 v128, v128 offset:4
	ds_read_b32 v129, v129 offset:4
	ds_read_b32 v130, v130 offset:4
	ds_read_b32 v131, v131 offset:4
	ds_read_b32 v132, v132 offset:4
	ds_read_b32 v133, v133 offset:4
	ds_read_b32 v134, v134 offset:4
	ds_read_b32 v135, v135 offset:4
	ds_read_b32 v136, v136 offset:4
	ds_read_b32 v137, v137 offset:4
	v_lshl_add_u32 v172, v168, 2, s33
	v_subrev_u32_e32 v168, 49, v64
	s_waitcnt lgkmcnt(14)
	v_med3_i32 v168, v168, -1, v232
	s_waitcnt lgkmcnt(13)
	s_waitcnt lgkmcnt(12)
	v_pk_add_f32 v[122:123], v[48:49], v[122:123]
	v_lshl_add_u32 v173, v168, 2, s33
	v_subrev_u32_e32 v168, 50, v64
	s_waitcnt lgkmcnt(11)
	s_waitcnt lgkmcnt(10)
	v_max3_f32 v138, v122, s23, v123
	v_pk_add_f32 v[124:125], v[50:51], v[124:125]
	v_med3_i32 v168, v168, -1, v232
	s_waitcnt lgkmcnt(9)
	s_waitcnt lgkmcnt(8)
	v_max3_f32 v138, v138, v124, v125
	v_pk_add_f32 v[126:127], v[52:53], v[126:127]
	v_lshl_add_u32 v174, v168, 2, s33
	v_subrev_u32_e32 v168, 51, v64
	s_waitcnt lgkmcnt(7)
	s_waitcnt lgkmcnt(6)
	v_max3_f32 v138, v138, v126, v127
	v_pk_add_f32 v[128:129], v[54:55], v[128:129]
	v_med3_i32 v168, v168, -1, v232
	s_waitcnt lgkmcnt(5)
	s_waitcnt lgkmcnt(4)
	v_max3_f32 v138, v138, v128, v129
	v_pk_add_f32 v[130:131], v[56:57], v[130:131]
	v_lshl_add_u32 v175, v168, 2, s33
	v_subrev_u32_e32 v168, 56, v64
	s_waitcnt lgkmcnt(3)
	s_waitcnt lgkmcnt(2)
	v_max3_f32 v138, v138, v130, v131
	v_pk_add_f32 v[132:133], v[58:59], v[132:133]
	v_med3_i32 v168, v168, -1, v232
	s_waitcnt lgkmcnt(1)
	s_waitcnt lgkmcnt(0)
	v_max3_f32 v138, v138, v132, v133
	v_pk_add_f32 v[134:135], v[60:61], v[134:135]
	v_lshl_add_u32 v203, v168, 2, s33
	v_subrev_u32_e32 v168, 57, v64
	v_max3_f32 v138, v138, v134, v135
	v_pk_add_f32 v[136:137], v[62:63], v[136:137]
	v_med3_i32 v168, v168, -1, v232
	v_max3_f32 v166, v138, v136, v137
	v_subrev_u32_e32 v138, 32, v64
	v_subrev_u32_e32 v139, 33, v64
	v_subrev_u32_e32 v140, 34, v64
	v_subrev_u32_e32 v141, 35, v64
	v_lshl_add_u32 v205, v168, 2, s33
	v_subrev_u32_e32 v168, 58, v64
	v_med3_i32 v138, v138, -1, v232
	v_med3_i32 v139, v139, -1, v232
	v_med3_i32 v140, v140, -1, v232
	v_med3_i32 v141, v141, -1, v232
	v_subrev_u32_e32 v164, 40, v64
	v_subrev_u32_e32 v165, 41, v64
	v_subrev_u32_e32 v167, 42, v64
	v_med3_i32 v168, v168, -1, v232
	v_subrev_u32_e32 v64, 59, v64
	v_lshl_add_u32 v138, v138, 2, s33
	v_lshl_add_u32 v139, v139, 2, s33
	v_lshl_add_u32 v140, v140, 2, s33
	v_lshl_add_u32 v141, v141, 2, s33
	v_med3_i32 v164, v164, -1, v232
	v_med3_i32 v165, v165, -1, v232
	v_med3_i32 v167, v167, -1, v232
	v_lshl_add_u32 v226, v168, 2, s33
	v_med3_i32 v64, v64, -1, v232
	v_lshl_add_u32 v164, v164, 2, s33
	v_lshl_add_u32 v165, v165, 2, s33
	v_lshl_add_u32 v167, v167, 2, s33
	v_lshl_add_u32 v64, v64, 2, s33
	ds_read_b32 v138, v138 offset:4
	ds_read_b32 v139, v139 offset:4
	ds_read_b32 v140, v140 offset:4
	ds_read_b32 v141, v141 offset:4
	ds_read_b32 v168, v164 offset:4
	ds_read_b32 v169, v165 offset:4
	ds_read_b32 v170, v167 offset:4
	ds_read_b32 v171, v171 offset:4
	ds_read_b32 v172, v172 offset:4
	ds_read_b32 v173, v173 offset:4
	ds_read_b32 v174, v174 offset:4
	ds_read_b32 v175, v175 offset:4
	ds_read_b32 v204, v203 offset:4
	ds_read_b32 v205, v205 offset:4
	ds_read_b32 v226, v226 offset:4
	ds_read_b32 v227, v64 offset:4
	s_waitcnt lgkmcnt(14)
	s_waitcnt lgkmcnt(13)
	s_waitcnt lgkmcnt(12)
	s_waitcnt lgkmcnt(11)
	s_waitcnt lgkmcnt(10)
	s_waitcnt lgkmcnt(9)
	v_pk_add_f32 v[164:165], v[32:33], v[138:139]
	s_waitcnt lgkmcnt(8)
	v_pk_add_f32 v[168:169], v[36:37], v[168:169]
	v_max3_f32 v64, v166, v164, v165
	v_pk_add_f32 v[166:167], v[34:35], v[140:141]
	s_waitcnt lgkmcnt(7)
	s_waitcnt lgkmcnt(6)
	v_pk_add_f32 v[170:171], v[38:39], v[170:171]
	v_max3_f32 v64, v64, v166, v167
	v_max3_f32 v64, v64, v168, v169
	s_waitcnt lgkmcnt(5)
	s_waitcnt lgkmcnt(4)
	v_max3_f32 v64, v64, v170, v171
	v_pk_add_f32 v[172:173], v[40:41], v[172:173]
	v_pk_add_f32 v[174:175], v[42:43], v[174:175]
	v_max3_f32 v64, v64, v172, v173
	s_waitcnt lgkmcnt(3)
	s_waitcnt lgkmcnt(2)
	v_max3_f32 v64, v64, v174, v175
	v_pk_add_f32 v[138:139], v[44:45], v[204:205]
	s_waitcnt lgkmcnt(1)
	s_waitcnt lgkmcnt(0)
	v_max3_f32 v64, v64, v138, v139
	v_pk_add_f32 v[140:141], v[46:47], v[226:227]
	s_nop 0
	v_max3_f32 v64, v64, v140, v141
	s_cbranch_execnz .LBB0_2233
